# P8: activation-tile DMA groups also issued at SP2 load-segment start (before LDS reads), wait vmcnt(8)
# baseline (speedup 1.0000x reference)
.LBB0_901:
	ds_read_b64_tr_b16 v[26:27], v207 offset:0
	ds_read_b64_tr_b16 v[28:29], v207 offset:1024
	ds_read_b64_tr_b16 v[30:31], v207 offset:8192
	ds_read_b64_tr_b16 v[32:33], v207 offset:9216
	ds_read_b64_tr_b16 v[18:19], v217 offset:0
	ds_read_b64_tr_b16 v[20:21], v217 offset:1024
	ds_read_b64_tr_b16 v[22:23], v217 offset:8192
	ds_read_b64_tr_b16 v[24:25], v217 offset:9216
	ds_read_b64_tr_b16 v[10:11], v214 offset:0
	ds_read_b64_tr_b16 v[12:13], v214 offset:1024
	ds_read_b64_tr_b16 v[14:15], v214 offset:8192
	ds_read_b64_tr_b16 v[16:17], v214 offset:9216
	ds_read_b64_tr_b16 v[2:3], v218 offset:0
	ds_read_b64_tr_b16 v[4:5], v218 offset:1024
	ds_read_b64_tr_b16 v[6:7], v218 offset:8192
	ds_read_b64_tr_b16 v[8:9], v218 offset:9216
	s_add_u32 s2, s50, 0xfffc0080
	s_addc_u32 s3, s51, -1
	s_cmp_eq_u32 s72, 12
	s_cselect_b32 s55, s29, s3
	s_cselect_b32 s54, s31, s2
	s_cselect_b32 s53, s35, s71
	s_cselect_b32 s52, s43, s70
	ds_read_b128 v[34:37], v223
	ds_read_b128 v[38:41], v223 offset:1024
	ds_read_b128 v[42:45], v223 offset:2048
	ds_read_b128 v[46:49], v223 offset:3072
	ds_read_b128 v[50:53], v223 offset:4096
	ds_read_b128 v[54:57], v223 offset:5120
	ds_read_b128 v[58:61], v223 offset:6144
	ds_read_b128 v[62:65], v223 offset:7168
	s_waitcnt vmcnt(6)
	s_waitcnt lgkmcnt(0)
	s_barrier
	s_setprio 1
	s_waitcnt lgkmcnt(0)
	v_mfma_scale_f32_16x16x128_f8f6f4 v[194:197], v[26:33], v[34:41], v[194:197], v1, v1 op_sel_hi:[0,0,0]
	v_mfma_scale_f32_16x16x128_f8f6f4 v[190:193], v[18:25], v[34:41], v[190:193], v1, v1 op_sel_hi:[0,0,0]
	v_mfma_scale_f32_16x16x128_f8f6f4 v[186:189], v[26:33], v[42:49], v[186:189], v1, v1 op_sel_hi:[0,0,0]
	v_mfma_scale_f32_16x16x128_f8f6f4 v[182:185], v[18:25], v[42:49], v[182:185], v1, v1 op_sel_hi:[0,0,0]
	v_lshl_add_u64 v[68:69], s[50:51], 0, v[208:209]
	s_add_i32 m0, s17, 0xc000
	s_nop 0
	global_load_lds_dwordx4 v[68:69], off
	v_mfma_scale_f32_16x16x128_f8f6f4 v[162:165], v[26:33], v[50:57], v[162:165], v1, v1 op_sel_hi:[0,0,0]
	v_mfma_scale_f32_16x16x128_f8f6f4 v[158:161], v[18:25], v[50:57], v[158:161], v1, v1 op_sel_hi:[0,0,0]
	v_mfma_scale_f32_16x16x128_f8f6f4 v[146:149], v[26:33], v[58:65], v[146:149], v1, v1 op_sel_hi:[0,0,0]
	v_mfma_scale_f32_16x16x128_f8f6f4 v[142:145], v[18:25], v[58:65], v[142:145], v1, v1 op_sel_hi:[0,0,0]
	s_setprio 0
	s_setprio 1
	v_mfma_scale_f32_16x16x128_f8f6f4 v[178:181], v[10:17], v[34:41], v[178:181], v1, v1 op_sel_hi:[0,0,0]
	v_mfma_scale_f32_16x16x128_f8f6f4 v[174:177], v[2:9], v[34:41], v[174:177], v1, v1 op_sel_hi:[0,0,0]
	v_lshl_add_u64 v[68:69], s[50:51], 0, v[210:211]
	s_add_i32 m0, s17, 0xe000
	s_nop 0
	global_load_lds_dwordx4 v[68:69], off
	v_mfma_scale_f32_16x16x128_f8f6f4 v[170:173], v[10:17], v[42:49], v[170:173], v1, v1 op_sel_hi:[0,0,0]
	v_mfma_scale_f32_16x16x128_f8f6f4 v[166:169], v[2:9], v[42:49], v[166:169], v1, v1 op_sel_hi:[0,0,0]
	v_mfma_scale_f32_16x16x128_f8f6f4 v[154:157], v[10:17], v[50:57], v[154:157], v1, v1 op_sel_hi:[0,0,0]
	v_mfma_scale_f32_16x16x128_f8f6f4 v[150:153], v[2:9], v[50:57], v[150:153], v1, v1 op_sel_hi:[0,0,0]
	v_mfma_scale_f32_16x16x128_f8f6f4 v[138:141], v[10:17], v[58:65], v[138:141], v1, v1 op_sel_hi:[0,0,0]
	v_mfma_scale_f32_16x16x128_f8f6f4 v[134:137], v[2:9], v[58:65], v[134:137], v1, v1 op_sel_hi:[0,0,0]
	s_setprio 0
	s_barrier
	s_mov_b32 m0, s19
	v_lshl_add_u64 v[68:69], s[52:53], 0, v[200:201]
	global_load_lds_dwordx4 v[68:69], off
	v_lshl_add_u64 v[212:213], s[52:53], 0, v[204:205]
	s_mov_b32 m0, s33
	v_lshl_add_u64 v[68:69], v[68:69], 0, s[4:5]
	global_load_lds_dwordx4 v[212:213], off
	s_mov_b32 m0, s45
	s_nop 0
	global_load_lds_dwordx4 v[68:69], off
	v_lshl_add_u64 v[68:69], v[212:213], 0, s[4:5]
	s_mov_b32 m0, s47
	v_lshl_add_u64 v[212:213], s[54:55], 0, v[202:203]
	global_load_lds_dwordx4 v[68:69], off
	v_lshl_add_u64 v[68:69], s[54:55], 0, v[198:199]
	s_mov_b32 m0, s17
	s_nop 0
	global_load_lds_dwordx4 v[68:69], off
	s_mov_b32 m0, s58
	s_nop 0
	global_load_lds_dwordx4 v[212:213], off
	s_andn2_b64 vcc, exec, s[48:49]
	s_cbranch_vccnz .Lhalfskip_p8a
	ds_read_b128 v[58:61], v223 offset:16384
	ds_read_b128 v[62:65], v223 offset:17408
	ds_read_b128 v[50:53], v223 offset:18432
	ds_read_b128 v[54:57], v223 offset:19456
	ds_read_b128 v[42:45], v223 offset:20480
	ds_read_b128 v[46:49], v223 offset:21504
	ds_read_b128 v[34:37], v223 offset:22528
	ds_read_b128 v[38:41], v223 offset:23552
.Lhalfskip_p8a:
	v_cmp_ne_u32_e64 s[2:3], 1, v225
	s_waitcnt vmcnt(8)
	s_waitcnt lgkmcnt(0)
	s_barrier
	s_cbranch_vccnz .Lp8_skip_b
	s_setprio 1
	s_waitcnt lgkmcnt(0)
	v_mfma_scale_f32_16x16x128_f8f6f4 v[130:133], v[26:33], v[58:65], v[130:133], v1, v1 op_sel_hi:[0,0,0]
	v_mfma_scale_f32_16x16x128_f8f6f4 v[126:129], v[18:25], v[58:65], v[126:129], v1, v1 op_sel_hi:[0,0,0]
	v_mfma_scale_f32_16x16x128_f8f6f4 v[114:117], v[26:33], v[50:57], v[114:117], v1, v1 op_sel_hi:[0,0,0]
	v_mfma_scale_f32_16x16x128_f8f6f4 v[110:113], v[18:25], v[50:57], v[110:113], v1, v1 op_sel_hi:[0,0,0]
	v_mfma_scale_f32_16x16x128_f8f6f4 v[98:101], v[26:33], v[42:49], v[98:101], v1, v1 op_sel_hi:[0,0,0]
	v_mfma_scale_f32_16x16x128_f8f6f4 v[94:97], v[18:25], v[42:49], v[94:97], v1, v1 op_sel_hi:[0,0,0]
	v_mfma_scale_f32_16x16x128_f8f6f4 v[82:85], v[26:33], v[34:41], v[82:85], v1, v1 op_sel_hi:[0,0,0]
	v_mfma_scale_f32_16x16x128_f8f6f4 v[78:81], v[18:25], v[34:41], v[78:81], v1, v1 op_sel_hi:[0,0,0]
	s_setprio 0
	s_setprio 1
	v_mfma_scale_f32_16x16x128_f8f6f4 v[122:125], v[10:17], v[58:65], v[122:125], v1, v1 op_sel_hi:[0,0,0]
	v_mfma_scale_f32_16x16x128_f8f6f4 v[118:121], v[2:9], v[58:65], v[118:121], v1, v1 op_sel_hi:[0,0,0]
	v_mfma_scale_f32_16x16x128_f8f6f4 v[106:109], v[10:17], v[50:57], v[106:109], v1, v1 op_sel_hi:[0,0,0]
	v_mfma_scale_f32_16x16x128_f8f6f4 v[102:105], v[2:9], v[50:57], v[102:105], v1, v1 op_sel_hi:[0,0,0]
	v_mfma_scale_f32_16x16x128_f8f6f4 v[90:93], v[10:17], v[42:49], v[90:93], v1, v1 op_sel_hi:[0,0,0]
	v_mfma_scale_f32_16x16x128_f8f6f4 v[86:89], v[2:9], v[42:49], v[86:89], v1, v1 op_sel_hi:[0,0,0]
	v_mfma_scale_f32_16x16x128_f8f6f4 v[74:77], v[10:17], v[34:41], v[74:77], v1, v1 op_sel_hi:[0,0,0]
	v_mfma_scale_f32_16x16x128_f8f6f4 v[70:73], v[2:9], v[34:41], v[70:73], v1, v1 op_sel_hi:[0,0,0]
	s_setprio 0
.LBB0_903:
	s_add_u32 s56, s52, 0x40000
	s_addc_u32 s57, s53, 0
	s_barrier
	ds_read_b64_tr_b16 v[26:27], v215 offset:0
	ds_read_b64_tr_b16 v[28:29], v215 offset:1024
	ds_read_b64_tr_b16 v[30:31], v215 offset:8192
	ds_read_b64_tr_b16 v[32:33], v215 offset:9216
	ds_read_b64_tr_b16 v[18:19], v219 offset:0
	ds_read_b64_tr_b16 v[20:21], v219 offset:1024
	ds_read_b64_tr_b16 v[22:23], v219 offset:8192
	ds_read_b64_tr_b16 v[24:25], v219 offset:9216
	ds_read_b64_tr_b16 v[10:11], v216 offset:0
	ds_read_b64_tr_b16 v[12:13], v216 offset:1024
	ds_read_b64_tr_b16 v[14:15], v216 offset:8192
	ds_read_b64_tr_b16 v[16:17], v216 offset:9216
	ds_read_b64_tr_b16 v[2:3], v220 offset:0
	ds_read_b64_tr_b16 v[4:5], v220 offset:1024
	ds_read_b64_tr_b16 v[6:7], v220 offset:8192
	ds_read_b64_tr_b16 v[8:9], v220 offset:9216
	s_add_u32 s54, s54, 0x40000
	s_addc_u32 s55, s55, 0
	ds_read_b128 v[34:37], v223 offset:32768
	ds_read_b128 v[38:41], v223 offset:33792
	ds_read_b128 v[42:45], v223 offset:34816
	ds_read_b128 v[46:49], v223 offset:35840
	ds_read_b128 v[50:53], v223 offset:36864
	ds_read_b128 v[54:57], v223 offset:37888
	ds_read_b128 v[58:61], v223 offset:38912
	ds_read_b128 v[62:65], v223 offset:39936
	s_waitcnt vmcnt(6)
	s_waitcnt lgkmcnt(0)
	s_barrier
	s_setprio 1
	s_waitcnt lgkmcnt(0)
	v_mfma_scale_f32_16x16x128_f8f6f4 v[194:197], v[26:33], v[34:41], v[194:197], v1, v1 op_sel_hi:[0,0,0]
	v_mfma_scale_f32_16x16x128_f8f6f4 v[190:193], v[18:25], v[34:41], v[190:193], v1, v1 op_sel_hi:[0,0,0]
	v_mfma_scale_f32_16x16x128_f8f6f4 v[186:189], v[26:33], v[42:49], v[186:189], v1, v1 op_sel_hi:[0,0,0]
	v_mfma_scale_f32_16x16x128_f8f6f4 v[182:185], v[18:25], v[42:49], v[182:185], v1, v1 op_sel_hi:[0,0,0]
	s_mov_b32 m0, s59
	v_lshl_add_u64 v[226:227], s[54:55], 0, v[198:199]
	global_load_lds_dwordx4 v[226:227], off
	v_mfma_scale_f32_16x16x128_f8f6f4 v[162:165], v[26:33], v[50:57], v[162:165], v1, v1 op_sel_hi:[0,0,0]
	v_mfma_scale_f32_16x16x128_f8f6f4 v[158:161], v[18:25], v[50:57], v[158:161], v1, v1 op_sel_hi:[0,0,0]
	v_mfma_scale_f32_16x16x128_f8f6f4 v[146:149], v[26:33], v[58:65], v[146:149], v1, v1 op_sel_hi:[0,0,0]
	v_mfma_scale_f32_16x16x128_f8f6f4 v[142:145], v[18:25], v[58:65], v[142:145], v1, v1 op_sel_hi:[0,0,0]
	s_setprio 0
	s_setprio 1
	v_mfma_scale_f32_16x16x128_f8f6f4 v[178:181], v[10:17], v[34:41], v[178:181], v1, v1 op_sel_hi:[0,0,0]
	v_mfma_scale_f32_16x16x128_f8f6f4 v[174:177], v[2:9], v[34:41], v[174:177], v1, v1 op_sel_hi:[0,0,0]
	v_lshl_add_u64 v[226:227], s[54:55], 0, v[202:203]
	s_mov_b32 m0, s60
	s_nop 0
	global_load_lds_dwordx4 v[226:227], off
	v_mfma_scale_f32_16x16x128_f8f6f4 v[170:173], v[10:17], v[42:49], v[170:173], v1, v1 op_sel_hi:[0,0,0]
	v_mfma_scale_f32_16x16x128_f8f6f4 v[166:169], v[2:9], v[42:49], v[166:169], v1, v1 op_sel_hi:[0,0,0]
	v_mfma_scale_f32_16x16x128_f8f6f4 v[154:157], v[10:17], v[50:57], v[154:157], v1, v1 op_sel_hi:[0,0,0]
	v_mfma_scale_f32_16x16x128_f8f6f4 v[150:153], v[2:9], v[50:57], v[150:153], v1, v1 op_sel_hi:[0,0,0]
	v_mfma_scale_f32_16x16x128_f8f6f4 v[138:141], v[10:17], v[58:65], v[138:141], v1, v1 op_sel_hi:[0,0,0]
	v_mfma_scale_f32_16x16x128_f8f6f4 v[134:137], v[2:9], v[58:65], v[134:137], v1, v1 op_sel_hi:[0,0,0]
	s_setprio 0
	s_barrier
	v_lshl_add_u64 v[226:227], s[56:57], 0, v[200:201]
	s_add_i32 m0, s17, 0x18000
	s_nop 0
	global_load_lds_dwordx4 v[226:227], off
	s_add_i32 m0, s17, 0x1a000
	v_lshl_add_u64 v[226:227], s[56:57], 0, v[204:205]
	global_load_lds_dwordx4 v[226:227], off
	s_add_u32 s52, s52, 0x40100
	s_addc_u32 s53, s53, 0
	v_lshl_add_u64 v[226:227], s[52:53], 0, v[200:201]
	s_add_i32 m0, s17, 0x1c000
	v_lshl_add_u64 v[68:69], v[68:69], 0, s[12:13]
	global_load_lds_dwordx4 v[226:227], off
	v_lshl_add_u64 v[226:227], s[52:53], 0, v[204:205]
	s_add_i32 m0, s17, 0x1e000
	s_nop 0
	global_load_lds_dwordx4 v[226:227], off
	s_mov_b32 m0, s62
	s_nop 0
	global_load_lds_dwordx4 v[68:69], off
	v_lshl_add_u64 v[68:69], v[212:213], 0, s[12:13]
	s_mov_b32 m0, s63
	s_nop 0
	global_load_lds_dwordx4 v[68:69], off
	s_and_b64 vcc, exec, s[2:3]
	s_cbranch_vccnz .Lhalfskip_p8b
	ds_read_b128 v[58:61], v223 offset:49152
	ds_read_b128 v[62:65], v223 offset:50176
	ds_read_b128 v[50:53], v223 offset:51200
	ds_read_b128 v[54:57], v223 offset:52224
	ds_read_b128 v[42:45], v223 offset:53248
	ds_read_b128 v[46:49], v223 offset:54272
	ds_read_b128 v[34:37], v223 offset:55296
	ds_read_b128 v[38:41], v223 offset:56320
.Lhalfskip_p8b:
	s_waitcnt vmcnt(8)
	s_waitcnt lgkmcnt(0)
	s_barrier
	s_cbranch_vccnz .Lp8_skip_d
	s_setprio 1
	s_waitcnt lgkmcnt(0)
	v_mfma_scale_f32_16x16x128_f8f6f4 v[130:133], v[26:33], v[58:65], v[130:133], v1, v1 op_sel_hi:[0,0,0]
	v_mfma_scale_f32_16x16x128_f8f6f4 v[126:129], v[18:25], v[58:65], v[126:129], v1, v1 op_sel_hi:[0,0,0]
	v_mfma_scale_f32_16x16x128_f8f6f4 v[114:117], v[26:33], v[50:57], v[114:117], v1, v1 op_sel_hi:[0,0,0]
	v_mfma_scale_f32_16x16x128_f8f6f4 v[110:113], v[18:25], v[50:57], v[110:113], v1, v1 op_sel_hi:[0,0,0]
	v_mfma_scale_f32_16x16x128_f8f6f4 v[98:101], v[26:33], v[42:49], v[98:101], v1, v1 op_sel_hi:[0,0,0]
	v_mfma_scale_f32_16x16x128_f8f6f4 v[94:97], v[18:25], v[42:49], v[94:97], v1, v1 op_sel_hi:[0,0,0]
	v_mfma_scale_f32_16x16x128_f8f6f4 v[82:85], v[26:33], v[34:41], v[82:85], v1, v1 op_sel_hi:[0,0,0]
	v_mfma_scale_f32_16x16x128_f8f6f4 v[78:81], v[18:25], v[34:41], v[78:81], v1, v1 op_sel_hi:[0,0,0]
	s_setprio 0
	s_setprio 1
	v_mfma_scale_f32_16x16x128_f8f6f4 v[122:125], v[10:17], v[58:65], v[122:125], v1, v1 op_sel_hi:[0,0,0]
	v_mfma_scale_f32_16x16x128_f8f6f4 v[118:121], v[2:9], v[58:65], v[118:121], v1, v1 op_sel_hi:[0,0,0]
	v_mfma_scale_f32_16x16x128_f8f6f4 v[106:109], v[10:17], v[50:57], v[106:109], v1, v1 op_sel_hi:[0,0,0]
	v_mfma_scale_f32_16x16x128_f8f6f4 v[102:105], v[2:9], v[50:57], v[102:105], v1, v1 op_sel_hi:[0,0,0]
	v_mfma_scale_f32_16x16x128_f8f6f4 v[90:93], v[10:17], v[42:49], v[90:93], v1, v1 op_sel_hi:[0,0,0]
	v_mfma_scale_f32_16x16x128_f8f6f4 v[86:89], v[2:9], v[42:49], v[86:89], v1, v1 op_sel_hi:[0,0,0]
	v_mfma_scale_f32_16x16x128_f8f6f4 v[74:77], v[10:17], v[34:41], v[74:77], v1, v1 op_sel_hi:[0,0,0]
	v_mfma_scale_f32_16x16x128_f8f6f4 v[70:73], v[2:9], v[34:41], v[70:73], v1, v1 op_sel_hi:[0,0,0]
	s_setprio 0
	s_branch .LBB0_900
.Lp8_skip_b:
	s_branch .LBB0_903
.Lp8_skip_d:
	s_branch .LBB0_900
.LBB0_905:
	s_and_b64 vcc, exec, s[14:15]
	s_cbranch_vccz .LBB0_907
	s_barrier
